# baseline (speedup 1.0000x reference)
_Z7xform_xPKfP15HIP_vector_typeIjLj4EE:
	s_load_dwordx4 s[4:7], s[0:1], 0x0
	s_bfe_u32 s1, s2, 0x20001
	s_and_b32 s3, s2, 1
	s_lshl_b32 s3, s3, 5
	s_lshr_b32 s0, s2, 3
	s_add_i32 s0, s0, s3
	v_lshrrev_b32_e32 v40, 4, v0
	v_bfe_u32 v2, v0, 4, 3
	v_lshl_or_b32 v32, s1, 3, v2
	v_lshlrev_b32_e32 v41, 2, v40
	v_and_b32_e32 v1, 15, v0
	v_mov_b32_e32 v35, 0
	v_and_or_b32 v2, v41, 32, v32
	v_lshlrev_b32_e32 v34, 4, v1
	v_lshl_add_u32 v18, v2, 6, s0
	v_mov_b32_e32 v19, v35
	s_waitcnt lgkmcnt(0)
	v_lshl_add_u64 v[26:27], s[4:5], 0, v[34:35]
	v_lshlrev_b64 v[2:3], 8, v[18:19]
	v_lshl_add_u64 v[10:11], v[26:27], 0, v[2:3]
	v_or_b32_e32 v2, 64, v41
	s_movk_i32 s2, 0x60
	v_and_or_b32 v2, v2, s2, v32
	v_lshl_add_u32 v2, v2, 6, s0
	v_mov_b32_e32 v3, v35
	v_lshlrev_b64 v[2:3], 8, v[2:3]
	v_lshl_add_u64 v[12:13], v[26:27], 0, v[2:3]
	global_load_dwordx4 v[2:5], v[10:11], off nt
	global_load_dwordx4 v[6:9], v[12:13], off nt
	v_or_b32_e32 v10, 0x80, v41
	s_movk_i32 s2, 0xa0
	v_and_or_b32 v10, v10, s2, v32
	v_lshl_add_u32 v10, v10, 6, s0
	v_mov_b32_e32 v11, v35
	v_lshlrev_b64 v[10:11], 8, v[10:11]
	v_add_u32_e32 v18, 0x4000, v18
	v_lshl_add_u64 v[20:21], v[26:27], 0, v[10:11]
	v_or_b32_e32 v10, 0xc0, v41
	s_movk_i32 s2, 0xe0
	v_lshlrev_b64 v[18:19], 8, v[18:19]
	v_and_or_b32 v10, v10, s2, v32
	v_lshl_add_u64 v[28:29], v[26:27], 0, v[18:19]
	v_or_b32_e32 v18, 0x140, v41
	s_movk_i32 s2, 0x160
	v_lshl_add_u32 v10, v10, 6, s0
	v_mov_b32_e32 v11, v35
	v_and_or_b32 v18, v18, s2, v32
	v_lshlrev_b64 v[10:11], 8, v[10:11]
	v_lshl_add_u32 v18, v18, 6, s0
	v_mov_b32_e32 v19, v35
	v_lshl_add_u64 v[22:23], v[26:27], 0, v[10:11]
	v_lshlrev_b64 v[18:19], 8, v[18:19]
	global_load_dwordx4 v[10:13], v[20:21], off nt
	global_load_dwordx4 v[14:17], v[22:23], off nt
	v_lshl_add_u64 v[30:31], v[26:27], 0, v[18:19]
	global_load_dwordx4 v[18:21], v[28:29], off nt
	global_load_dwordx4 v[22:25], v[30:31], off nt
	v_or_b32_e32 v28, 0x180, v41
	s_movk_i32 s2, 0x1a0
	v_and_or_b32 v28, v28, s2, v32
	v_lshl_add_u32 v28, v28, 6, s0
	v_mov_b32_e32 v29, v35
	v_lshlrev_b64 v[28:29], 8, v[28:29]
	v_lshl_add_u64 v[36:37], v[26:27], 0, v[28:29]
	v_or_b32_e32 v28, 0x1c0, v41
	s_movk_i32 s2, 0x1e0
	v_and_or_b32 v28, v28, s2, v32
	v_lshl_add_u32 v28, v28, 6, s0
	v_mov_b32_e32 v29, v35
	v_lshlrev_b64 v[28:29], 8, v[28:29]
	v_lshl_add_u64 v[38:39], v[26:27], 0, v[28:29]
	global_load_dwordx4 v[26:29], v[36:37], off nt
	global_load_dwordx4 v[30:33], v[38:39], off nt
	s_movk_i32 s2, 0x110
	v_mul_u32_u24_e32 v36, 0x880, v1
	v_mad_u32_u24 v37, v40, s2, v34
	s_lshl_b32 s4, s0, 6
	s_lshl_b32 s0, s1, 8
	s_add_u32 s0, s6, s0
	s_addc_u32 s1, s7, 0
	s_movk_i32 s3, 0x880
	s_waitcnt vmcnt(7)
	ds_write_b128 v37, v[2:5]
	s_waitcnt vmcnt(6)
	ds_write_b128 v37, v[6:9] offset:4352
	s_waitcnt vmcnt(5)
	ds_write_b128 v37, v[10:13] offset:8704
	s_waitcnt vmcnt(4)
	ds_write_b128 v37, v[14:17] offset:13056
	s_waitcnt vmcnt(3)
	ds_write_b128 v37, v[18:21] offset:17408
	s_waitcnt vmcnt(2)
	ds_write_b128 v37, v[22:25] offset:21760
	s_waitcnt vmcnt(1)
	ds_write_b128 v37, v[26:29] offset:26112
	s_waitcnt vmcnt(0)
	ds_write_b128 v37, v[30:33] offset:30464
	v_or_b32_e32 v6, v36, v41
	v_add_u32_e32 v8, 0x400, v6
	s_waitcnt lgkmcnt(0)
	s_barrier
	ds_read2_b32 v[2:3], v6 offset1:68
	ds_read2_b32 v[4:5], v6 offset0:136 offset1:204
	ds_read2_b32 v[6:7], v8 offset0:16 offset1:84
	ds_read2_b32 v[8:9], v8 offset0:152 offset1:220
	v_lshl_add_u64 v[10:11], s[0:1], 0, v[34:35]
	v_or_b32_e32 v34, s4, v40
	s_waitcnt lgkmcnt(3)
	v_cvt_pk_f16_f32 v2, v2, v3
	s_waitcnt lgkmcnt(2)
	v_cvt_pk_f16_f32 v3, v4, v5
	s_waitcnt lgkmcnt(0)
	v_cvt_pk_f16_f32 v5, v8, v9
	v_or_b32_e32 v8, 0x100, v0
	v_lshrrev_b32_e32 v18, 4, v8
	v_lshl_or_b32 v14, v18, 2, v36
	ds_read2_b32 v[8:9], v14 offset1:68
	ds_read2_b32 v[12:13], v14 offset0:136 offset1:204
	v_cvt_pk_f16_f32 v4, v6, v7
	v_lshlrev_b64 v[6:7], 10, v[34:35]
	v_add_u32_e32 v16, 0x400, v14
	v_lshl_add_u64 v[6:7], v[10:11], 0, v[6:7]
	ds_read2_b32 v[14:15], v16 offset0:16 offset1:84
	ds_read2_b32 v[16:17], v16 offset0:152 offset1:220
	global_store_dwordx4 v[6:7], v[2:5], off
	v_or_b32_e32 v34, s4, v18
	v_lshlrev_b64 v[6:7], 10, v[34:35]
	s_waitcnt lgkmcnt(3)
	v_cvt_pk_f16_f32 v2, v8, v9
	v_or_b32_e32 v8, 0x200, v0
	v_lshrrev_b32_e32 v18, 4, v8
	v_lshlrev_b32_e32 v8, 2, v18
	s_waitcnt lgkmcnt(1)
	v_cvt_pk_f16_f32 v4, v14, v15
	v_mad_u32_u24 v14, v1, s3, v8
	s_waitcnt lgkmcnt(0)
	v_cvt_pk_f16_f32 v5, v16, v17
	v_add_u32_e32 v16, 0x400, v14
	v_cvt_pk_f16_f32 v3, v12, v13
	ds_read2_b32 v[8:9], v14 offset1:68
	ds_read2_b32 v[12:13], v14 offset0:136 offset1:204
	ds_read2_b32 v[14:15], v16 offset0:16 offset1:84
	ds_read2_b32 v[16:17], v16 offset0:152 offset1:220
	v_lshl_add_u64 v[6:7], v[10:11], 0, v[6:7]
	v_or_b32_e32 v0, 0x300, v0
	global_store_dwordx4 v[6:7], v[2:5], off
	v_or_b32_e32 v34, s4, v18
	v_lshlrev_b64 v[6:7], 10, v[34:35]
	s_waitcnt lgkmcnt(0)
	v_cvt_pk_f16_f32 v5, v16, v17
	v_lshrrev_b32_e32 v16, 4, v0
	v_lshlrev_b32_e32 v0, 2, v16
	v_cvt_pk_f16_f32 v3, v12, v13
	v_mad_u32_u24 v12, v1, s3, v0
	v_cvt_pk_f16_f32 v4, v14, v15
	v_add_u32_e32 v14, 0x400, v12
	v_cvt_pk_f16_f32 v2, v8, v9
	ds_read2_b32 v[0:1], v12 offset1:68
	ds_read2_b32 v[8:9], v12 offset0:136 offset1:204
	ds_read2_b32 v[12:13], v14 offset0:16 offset1:84
	ds_read2_b32 v[14:15], v14 offset0:152 offset1:220
	v_lshl_add_u64 v[6:7], v[10:11], 0, v[6:7]
	v_or_b32_e32 v34, s4, v16
	global_store_dwordx4 v[6:7], v[2:5], off
	s_waitcnt lgkmcnt(3)
	v_cvt_pk_f16_f32 v0, v0, v1
	s_waitcnt lgkmcnt(2)
	v_cvt_pk_f16_f32 v1, v8, v9
	v_lshlrev_b64 v[4:5], 10, v[34:35]
	s_waitcnt lgkmcnt(1)
	v_cvt_pk_f16_f32 v2, v12, v13
	s_waitcnt lgkmcnt(0)
	v_cvt_pk_f16_f32 v3, v14, v15
	v_lshl_add_u64 v[4:5], v[10:11], 0, v[4:5]
	global_store_dwordx4 v[4:5], v[0:3], off
	s_endpgm
